# adds: scan-A step-2 LDS reads issued up front; scan-C remembers last polled progress flag and skips the blocking poll (no vmcnt(0) drain) when already satisfied
# baseline (speedup 1.0000x reference)
; DI float bflo(unsigned w) { return __uint_as_float(w << 16); }
; DI float bfhi(unsigned w) { return __uint_as_float(w & 0xffff0000u); }
; DI void phase_scan_a(Frame& F, int l, int u_lo, int u_hi, int u_step) {
;     ...
;           float off = 0.f;
; #pragma unroll
;           for (int s = 0; s < 8; ++s) off += (s < seg) ? SEG[s * 64 + k] : 0.f;
; #pragma unroll
;           for (int e = 0; e < 8; ++e) Gf[(8 * seg + e) * GP + k] = off + p[e];
;         }
;         __syncthreads();
;         { const int i = F.tid >> 3, k0 = (F.tid & 7) * 8;
;           const u32x4 rv = prv, kv = pkv, av = pav, bv = pbv, vv = pvv;
;           float fr[8], fk[8], fa[8], fb[8], fv[8];
;           const unsigned rw[4] = {rv.x, rv.y, rv.z, rv.w}, kw[4] = {kv.x, kv.y, kv.z, kv.w}, aw[4] = {av.x, av.y, av.z, av.w}, bw[4] = {bv.x, bv.y, bv.z, bv.w}, vw[4] = {vv.x, vv.y, vv.z, vv.w};
; #pragma unroll
;           for (int q = 0; q < 4; ++q) { fr[2 * q] = bflo(rw[q]); fr[2 * q + 1] = bfhi(rw[q]); fk[2 * q] = bflo(kw[q]); fk[2 * q + 1] = bfhi(kw[q]); fa[2 * q] = bflo(aw[q]); fa[2 * q + 1] = bfhi(aw[q]);
;               fb[2 * q] = bflo(bw[q]); fb[2 * q + 1] = bfhi(bw[q]); fv[2 * q] = bflo(vw[q]); fv[2 * q + 1] = bfhi(vw[q]); }
;           float at[8], rt[8], bt[8], kt[8], bh8[8], kh8[8];
; #pragma unroll
;           for (int e = 0; e < 8; ++e) { const float gi = Gf[i * GP + k0 + e], gp = (i > 0) ? Gf[(i - 1) * GP + k0 + e] : 0.f, gl = Gf[63 * GP + k0 + e];
;               const float e1 = __expf(gp), e2 = __expf(gi), e3 = __expf(-gi), e4 = __expf(gl - gi);
;               at[e] = -fa[e] * e1; rt[e] = fr[e] * e2; bt[e] = fb[e] * e3; kt[e] = fk[e] * e3; bh8[e] = fb[e] * e4; kh8[e] = fk[e] * e4;
;               if (i == 63) GL[k0 + e] = e2; }
.LBB0_1016:
	s_or_b64 exec, exec, s[40:41]
	s_and_saveexec_b64 s[40:41], s[16:17]
	ds_read_b32 v28, v187 offset:256
	s_or_b64 exec, exec, s[40:41]
	v_mov_b32_e32 v30, 0
	v_mov_b32_e32 v31, 0
	s_and_saveexec_b64 s[40:41], s[18:19]
	ds_read_b32 v31, v187 offset:512
	s_or_b64 exec, exec, s[40:41]
	s_and_saveexec_b64 s[40:41], s[20:21]
	ds_read_b32 v30, v187 offset:768
	s_or_b64 exec, exec, s[40:41]
	v_mov_b32_e32 v32, 0
	v_mov_b32_e32 v33, 0
	s_and_saveexec_b64 s[40:41], s[22:23]
	ds_read_b32 v33, v187 offset:1024
	s_or_b64 exec, exec, s[40:41]
	s_and_saveexec_b64 s[40:41], s[26:27]
	ds_read_b32 v32, v187 offset:1280
	s_or_b64 exec, exec, s[40:41]
	v_mov_b32_e32 v34, 0
	v_mov_b32_e32 v35, 0
	s_and_saveexec_b64 s[40:41], s[28:29]
	ds_read_b32 v35, v187 offset:1536
	s_or_b64 exec, exec, s[40:41]
	s_and_saveexec_b64 s[40:41], s[30:31]
	ds_read_b32 v34, v187 offset:1792
	s_or_b64 exec, exec, s[40:41]
	s_waitcnt lgkmcnt(0)
	v_add_f32_e32 v28, v29, v28
	v_add_f32_e32 v28, v28, v31
	v_add_f32_e32 v28, v28, v30
	v_add_f32_e32 v28, v28, v33
	v_add_f32_e32 v28, v28, v32
	v_add_f32_e32 v28, v28, v35
	v_add_f32_e32 v28, v28, v34
	v_add_f32_e32 v24, v24, v28
	v_add_f32_e32 v25, v25, v28
	v_add_f32_e32 v26, v26, v28
	v_add_f32_e32 v27, v27, v28
	ds_write2_b32 v189, v24, v25 offset0:136 offset1:204
	v_add_f32_e32 v22, v22, v28
	v_add_f32_e32 v23, v23, v28
	v_add_u32_e32 v24, 0x400, v189
	v_add_f32_e32 v20, v20, v28
	v_add_f32_e32 v21, v21, v28
	ds_write2_b32 v189, v26, v27 offset1:68
	ds_write2_b32 v24, v22, v23 offset0:16 offset1:84
	ds_write2_b32 v24, v20, v21 offset0:152 offset1:220
	s_waitcnt lgkmcnt(0)
	s_barrier
	v_mov_b32_e32 v21, 0
	v_mov_b32_e32 v25, 0
	v_mov_b32_e32 v29, 0
	v_mov_b32_e32 v33, 0
	v_mov_b32_e32 v37, 0
	v_mov_b32_e32 v41, 0
	v_mov_b32_e32 v45, 0
	v_mov_b32_e32 v49, 0
	ds_read_b32 v20, v124
	ds_read_b32 v24, v124 offset:4
	ds_read_b32 v28, v124 offset:8
	ds_read_b32 v32, v124 offset:12
	ds_read_b32 v36, v124 offset:16
	ds_read_b32 v40, v124 offset:20
	ds_read_b32 v44, v124 offset:24
	ds_read_b32 v48, v124 offset:28
	s_and_saveexec_b64 s[40:41], s[34:35]
	ds_read_b32 v21, v125
	ds_read_b32 v25, v125 offset:4
	ds_read_b32 v29, v125 offset:8
	ds_read_b32 v33, v125 offset:12
	ds_read_b32 v37, v125 offset:16
	ds_read_b32 v41, v125 offset:20
	ds_read_b32 v45, v125 offset:24
	ds_read_b32 v49, v125 offset:28
	s_or_b64 exec, exec, s[40:41]
	ds_read_b32 v23, v122 offset:17136
	ds_read_b32 v27, v122 offset:17140
	ds_read_b32 v31, v122 offset:17144
	ds_read_b32 v35, v122 offset:17148
	ds_read_b32 v39, v122 offset:17152
	ds_read_b32 v43, v122 offset:17156
	ds_read_b32 v47, v122 offset:17160
	ds_read_b32 v51, v122 offset:17164
	s_waitcnt lgkmcnt(8)
	v_mul_f32_e32 v22, 0x3fb8aa3b, v20
	v_mul_f32_e32 v26, 0x3fb8aa3b, v24
	v_mul_f32_e32 v30, 0x3fb8aa3b, v28
	v_mul_f32_e32 v34, 0x3fb8aa3b, v32
	v_mul_f32_e32 v38, 0x3fb8aa3b, v36
	v_mul_f32_e32 v42, 0x3fb8aa3b, v40
	v_mul_f32_e32 v46, 0x3fb8aa3b, v44
	v_mul_f32_e32 v50, 0x3fb8aa3b, v48
	v_mul_f32_e32 v21, 0x3fb8aa3b, v21
	v_exp_f32_e32 v22, v22
	v_mul_f32_e32 v25, 0x3fb8aa3b, v25
	v_exp_f32_e32 v26, v26
	v_mul_f32_e32 v29, 0x3fb8aa3b, v29
	v_exp_f32_e32 v30, v30
	v_mul_f32_e32 v33, 0x3fb8aa3b, v33
	v_exp_f32_e32 v34, v34
	v_mul_f32_e32 v37, 0x3fb8aa3b, v37
	v_exp_f32_e32 v38, v38
	v_mul_f32_e32 v41, 0x3fb8aa3b, v41
	v_exp_f32_e32 v42, v42
	v_mul_f32_e32 v45, 0x3fb8aa3b, v45
	v_exp_f32_e32 v46, v46
	v_mul_f32_e32 v49, 0x3fb8aa3b, v49
	v_exp_f32_e32 v50, v50
	s_and_saveexec_b64 s[40:41], s[36:37]
	ds_write_b32 v188, v22
	ds_write_b32 v188, v26 offset:4
	ds_write_b32 v188, v30 offset:8
	ds_write_b32 v188, v34 offset:12
	ds_write_b32 v188, v38 offset:16
	ds_write_b32 v188, v42 offset:20
	ds_write_b32 v188, v46 offset:24
	ds_write_b32 v188, v50 offset:28
	s_or_b64 exec, exec, s[40:41]
	v_mul_f32_e32 v56, 0xbfb8aa3b, v48
	s_waitcnt lgkmcnt(0)
	v_sub_f32_e32 v48, v51, v48
	v_mul_f32_e32 v48, 0x3fb8aa3b, v48
	v_mul_f32_e32 v58, 0xbfb8aa3b, v44
	v_sub_f32_e32 v44, v47, v44
	v_exp_f32_e32 v49, v49
	v_exp_f32_e32 v56, v56
	v_exp_f32_e32 v48, v48
	v_mul_f32_e32 v44, 0x3fb8aa3b, v44
	v_mul_f32_e32 v60, 0xbfb8aa3b, v40
	v_sub_f32_e32 v40, v43, v40
	v_exp_f32_e32 v45, v45
	v_exp_f32_e32 v58, v58
	v_exp_f32_e32 v44, v44
	v_mul_f32_e32 v40, 0x3fb8aa3b, v40
	v_mul_f32_e32 v62, 0xbfb8aa3b, v36
	v_sub_f32_e32 v36, v39, v36
	v_exp_f32_e32 v41, v41
	v_exp_f32_e32 v60, v60
	v_exp_f32_e32 v40, v40
	v_mul_f32_e32 v36, 0x3fb8aa3b, v36
	v_mul_f32_e32 v66, 0xbfb8aa3b, v32
	v_sub_f32_e32 v32, v35, v32
	s_waitcnt vmcnt(4)
	v_and_b32_e32 v52, 0xffff0000, v3
	s_waitcnt vmcnt(3)
	v_and_b32_e32 v53, 0xffff0000, v7
	s_waitcnt vmcnt(2)
	v_and_b32_e32 v54, 0xffff0000, v11
	s_waitcnt vmcnt(1)
; #define LAS __attribute__((address_space(3)))
; DI unsigned pk2(float lo, float hi) { f32x2 v = {lo, hi}; return __builtin_bit_cast(unsigned, __builtin_convertvector(v, bf16v2)); }
; DI float bflo(unsigned w) { return __uint_as_float(w << 16); }
; DI float bfhi(unsigned w) { return __uint_as_float(w & 0xffff0000u); }
; DI void phase_scan_a(Frame& F, int l, int u_lo, int u_hi, int u_step) {
;     ...
;           for (int q = 0; q < 4; ++q) { fr[2 * q] = bflo(rw[q]); fr[2 * q + 1] = bfhi(rw[q]); fk[2 * q] = bflo(kw[q]); fk[2 * q + 1] = bfhi(kw[q]); fa[2 * q] = bflo(aw[q]); fa[2 * q + 1] = bfhi(aw[q]);
;               fb[2 * q] = bflo(bw[q]); fb[2 * q + 1] = bfhi(bw[q]); fv[2 * q] = bflo(vw[q]); fv[2 * q + 1] = bfhi(vw[q]); }
;           float at[8], rt[8], bt[8], kt[8], bh8[8], kh8[8];
; #pragma unroll
;           for (int e = 0; e < 8; ++e) { const float gi = Gf[i * GP + k0 + e], gp = (i > 0) ? Gf[(i - 1) * GP + k0 + e] : 0.f, gl = Gf[63 * GP + k0 + e];
;               const float e1 = __expf(gp), e2 = __expf(gi), e3 = __expf(-gi), e4 = __expf(gl - gi);
;               at[e] = -fa[e] * e1; rt[e] = fr[e] * e2; bt[e] = fb[e] * e3; kt[e] = fk[e] * e3; bh8[e] = fb[e] * e4; kh8[e] = fk[e] * e4;
;               if (i == 63) GL[k0 + e] = e2; }
;           u32x4 w;
;           w.x = pk2(at[0], at[1]); w.y = pk2(at[2], at[3]); w.z = pk2(at[4], at[5]); w.w = pk2(at[6], at[7]); *(LAS u32x4*)(MB(0) + i * MP + k0 * 2) = w;
;           w.x = pk2(rt[0], rt[1]); w.y = pk2(rt[2], rt[3]); w.z = pk2(rt[4], rt[5]); w.w = pk2(rt[6], rt[7]); *(LAS u32x4*)(MB(1) + i * MP + k0 * 2) = w;
;           w.x = pk2(bt[0], bt[1]); w.y = pk2(bt[2], bt[3]); w.z = pk2(bt[4], bt[5]); w.w = pk2(bt[6], bt[7]); *(LAS u32x4*)(MB(2) + i * MP + k0 * 2) = w;
;           w.x = pk2(kt[0], kt[1]); w.y = pk2(kt[2], kt[3]); w.z = pk2(kt[4], kt[5]); w.w = pk2(kt[6], kt[7]); *(LAS u32x4*)(MB(3) + i * MP + k0 * 2) = w;
;           { const int sel = i & 1;
; #pragma unroll
;             for (int q = 0; q < 4; ++q) { const int row = k0 + 4 * sel + q; const int ro = row * MP + (((i >> 3) ^ ((row >> 4) & 3)) << 4) + (i & 6) * 2;
;     ...
;                 TW(MB(4), at) TW(MB(5), fv) TW(MB(6), bh8) TW(MB(7), kh8)
	v_and_b32_e32 v55, 0xffff0000, v15
	v_exp_f32_e32 v37, v37
	v_exp_f32_e32 v62, v62
	v_exp_f32_e32 v36, v36
	v_mul_f32_e32 v32, 0x3fb8aa3b, v32
	v_mul_f32_e32 v68, 0xbfb8aa3b, v28
	v_sub_f32_e32 v28, v31, v28
	v_mul_f32_e64 v49, v49, -v54
	v_mul_f32_e32 v50, v50, v52
	v_mul_f32_e32 v51, v56, v55
	v_mul_f32_e32 v52, v56, v53
	v_mul_f32_e32 v54, v48, v55
	v_mul_f32_e32 v48, v48, v53
	v_lshlrev_b32_e32 v53, 16, v3
	v_lshlrev_b32_e32 v55, 16, v7
	v_lshlrev_b32_e32 v56, 16, v11
	v_lshlrev_b32_e32 v57, 16, v15
	v_exp_f32_e32 v33, v33
	v_exp_f32_e32 v66, v66
	v_exp_f32_e32 v32, v32
	v_mul_f32_e32 v28, 0x3fb8aa3b, v28
	v_mul_f32_e64 v45, v45, -v56
	v_mul_f32_e32 v46, v46, v53
	v_mul_f32_e32 v47, v58, v57
	v_mul_f32_e32 v53, v58, v55
	v_mul_f32_e32 v56, v44, v57
	v_mul_f32_e32 v44, v44, v55
	v_and_b32_e32 v55, 0xffff0000, v2
	v_and_b32_e32 v57, 0xffff0000, v6
	v_and_b32_e32 v58, 0xffff0000, v10
	v_and_b32_e32 v59, 0xffff0000, v14
	v_exp_f32_e32 v29, v29
	v_exp_f32_e32 v68, v68
	v_exp_f32_e32 v28, v28
	v_mul_f32_e32 v70, 0xbfb8aa3b, v24
	v_sub_f32_e32 v24, v27, v24
	v_mul_f32_e64 v41, v41, -v58
	v_mul_f32_e32 v42, v42, v55
	v_mul_f32_e32 v43, v60, v59
	v_mul_f32_e32 v55, v60, v57
	v_mul_f32_e32 v58, v40, v59
	v_mul_f32_e32 v40, v40, v57
	v_lshlrev_b32_e32 v57, 16, v2
	v_lshlrev_b32_e32 v59, 16, v6
	v_lshlrev_b32_e32 v60, 16, v10
	v_lshlrev_b32_e32 v61, 16, v14
	v_exp_f32_e32 v70, v70
	v_mul_f32_e32 v24, 0x3fb8aa3b, v24
	v_mul_f32_e32 v72, 0xbfb8aa3b, v20
	v_sub_f32_e32 v20, v23, v20
	v_mul_f32_e64 v37, v37, -v60
	v_mul_f32_e32 v38, v38, v57
	v_mul_f32_e32 v39, v62, v61
	v_mul_f32_e32 v57, v62, v59
	v_mul_f32_e32 v60, v36, v61
	v_mul_f32_e32 v36, v36, v59
	v_and_b32_e32 v59, 0xffff0000, v1
	v_and_b32_e32 v61, 0xffff0000, v5
	v_and_b32_e32 v62, 0xffff0000, v9
	v_and_b32_e32 v63, 0xffff0000, v13
	v_exp_f32_e32 v25, v25
	v_exp_f32_e32 v24, v24
	v_exp_f32_e32 v21, v21
	v_mul_f32_e32 v20, 0x3fb8aa3b, v20
	v_mul_f32_e64 v33, v33, -v62
	v_mul_f32_e32 v34, v34, v59
	v_mul_f32_e32 v35, v66, v63
	v_mul_f32_e32 v59, v66, v61
	v_mul_f32_e32 v62, v32, v63
	v_mul_f32_e32 v32, v32, v61
	v_lshlrev_b32_e32 v61, 16, v1
	v_lshlrev_b32_e32 v63, 16, v5
	v_lshlrev_b32_e32 v66, 16, v9
	v_lshlrev_b32_e32 v67, 16, v13
	v_exp_f32_e32 v72, v72
	v_exp_f32_e32 v20, v20
	v_mul_f32_e64 v29, v29, -v66
	v_mul_f32_e32 v30, v30, v61
	v_mul_f32_e32 v31, v68, v67
	v_mul_f32_e32 v61, v68, v63
	v_mul_f32_e32 v66, v28, v67
	v_mul_f32_e32 v28, v28, v63
	v_and_b32_e32 v63, 0xffff0000, v0
	v_and_b32_e32 v67, 0xffff0000, v4
	v_and_b32_e32 v69, 0xffff0000, v12
	v_and_b32_e32 v68, 0xffff0000, v8
	v_mul_f32_e32 v26, v26, v63
	v_mul_f32_e32 v27, v70, v69
	v_mul_f32_e32 v63, v70, v67
	v_lshlrev_b32_e32 v70, 16, v8
	v_mul_f32_e64 v25, v25, -v68
	v_mul_f32_e32 v68, v24, v69
	v_mul_f32_e32 v24, v24, v67
	v_lshlrev_b32_e32 v67, 16, v0
	v_lshlrev_b32_e32 v69, 16, v4
	v_lshlrev_b32_e32 v71, 16, v12
	v_mul_f32_e64 v70, v21, -v70
	v_mul_f32_e32 v67, v22, v67
	v_mul_f32_e32 v73, v72, v71
	v_mul_f32_e32 v72, v72, v69
	v_mul_f32_e32 v71, v20, v71
	v_mul_f32_e32 v69, v20, v69
	v_cvt_pk_bf16_f32 v20, v70, v25
	v_cvt_pk_bf16_f32 v21, v29, v33
	v_cvt_pk_bf16_f32 v22, v37, v41
	v_cvt_pk_bf16_f32 v23, v45, v49
	ds_write_b128 v190, v[20:23]
	v_cvt_pk_bf16_f32 v20, v67, v26
	v_cvt_pk_bf16_f32 v21, v30, v34
	v_cvt_pk_bf16_f32 v22, v38, v42
	v_cvt_pk_bf16_f32 v23, v46, v50
	ds_write_b128 v190, v[20:23] offset:9216
	v_cvt_pk_bf16_f32 v20, v73, v27
	v_cvt_pk_bf16_f32 v21, v31, v35
	v_cvt_pk_bf16_f32 v22, v39, v43
	v_cvt_pk_bf16_f32 v23, v47, v51
	ds_write_b128 v190, v[20:23] offset:18432
	v_cvt_pk_bf16_f32 v20, v72, v63
	v_cvt_pk_bf16_f32 v21, v61, v59
	v_cvt_pk_bf16_f32 v22, v57, v55
	v_cvt_pk_bf16_f32 v23, v53, v52
	ds_write_b128 v190, v[20:23] offset:27648
	v_mov_b32_dpp v20, v70 row_ror:8 row_mask:0xf bank_mask:0xf bound_ctrl:1
	v_mov_b32_dpp v21, v37 row_ror:8 row_mask:0xf bank_mask:0xf bound_ctrl:1
	v_cndmask_b32_e64 v20, v21, v20, s[38:39]
	s_waitcnt vmcnt(0)
	v_lshlrev_b32_e32 v74, 16, v16
	v_lshlrev_b32_e32 v78, 16, v18
	v_cndmask_b32_e64 v21, v20, v70, s[38:39]
	v_cndmask_b32_e64 v20, v37, v20, s[38:39]
	v_cvt_pk_bf16_f32 v20, v21, v20
	v_mov_b32_dpp v21, v74 row_ror:8 row_mask:0xf bank_mask:0xf bound_ctrl:1
	v_mov_b32_dpp v22, v78 row_ror:8 row_mask:0xf bank_mask:0xf bound_ctrl:1
	v_cndmask_b32_e64 v21, v22, v21, s[38:39]
	v_cndmask_b32_e64 v22, v21, v74, s[38:39]
	v_cndmask_b32_e64 v21, v78, v21, s[38:39]
	v_cvt_pk_bf16_f32 v21, v22, v21
	v_mov_b32_dpp v22, v71 row_ror:8 row_mask:0xf bank_mask:0xf bound_ctrl:1
	v_mov_b32_dpp v23, v60 row_ror:8 row_mask:0xf bank_mask:0xf bound_ctrl:1
	v_cndmask_b32_e64 v22, v23, v22, s[38:39]
	v_cndmask_b32_e64 v23, v22, v71, s[38:39]
	v_cndmask_b32_e64 v22, v60, v22, s[38:39]
	v_cvt_pk_bf16_f32 v22, v23, v22
	v_mov_b32_dpp v23, v69 row_ror:8 row_mask:0xf bank_mask:0xf bound_ctrl:1
	v_mov_b32_dpp v26, v36 row_ror:8 row_mask:0xf bank_mask:0xf bound_ctrl:1
	v_cndmask_b32_e64 v23, v26, v23, s[38:39]
	v_cndmask_b32_e64 v26, v23, v69, s[38:39]
	v_cndmask_b32_e64 v23, v36, v23, s[38:39]
	v_cvt_pk_bf16_f32 v23, v26, v23
	v_mov_b32_dpp v26, v25 row_ror:8 row_mask:0xf bank_mask:0xf bound_ctrl:1
	v_mov_b32_dpp v27, v41 row_ror:8 row_mask:0xf bank_mask:0xf bound_ctrl:1
	v_cndmask_b32_e64 v26, v27, v26, s[38:39]
	v_cndmask_b32_e64 v25, v26, v25, s[38:39]
	v_cndmask_b32_e64 v26, v41, v26, s[38:39]
	v_and_b32_e32 v75, 0xffff0000, v16
	v_and_b32_e32 v79, 0xffff0000, v18
	v_cvt_pk_bf16_f32 v25, v25, v26
	v_add_u32_e32 v26, 0x9000, v191
	ds_write2_b32 v26, v20, v25 offset1:36
	v_mov_b32_dpp v20, v75 row_ror:8 row_mask:0xf bank_mask:0xf bound_ctrl:1
	v_mov_b32_dpp v25, v79 row_ror:8 row_mask:0xf bank_mask:0xf bound_ctrl:1
; #define TW(dst, arr) { const float d0_ = dpp_mov<0x128>(arr[q]), d1_ = dpp_mov<0x128>(arr[4 + q]);     \
;                        const float m_ = sel ? arr[4 + q] : arr[q], o_ = sel ? d1_ : d0_; *(LAS unsigned*)(dst + ro) = pk2(sel ? o_ : m_, sel ? m_ : o_); }
; DI void phase_scan_a(Frame& F, int l, int u_lo, int u_hi, int u_step) {
;     ...
;           { const int sel = i & 1;
; #pragma unroll
;             for (int q = 0; q < 4; ++q) { const int row = k0 + 4 * sel + q; const int ro = row * MP + (((i >> 3) ^ ((row >> 4) & 3)) << 4) + (i & 6) * 2;
;     ...
;                 TW(MB(4), at) TW(MB(5), fv) TW(MB(6), bh8) TW(MB(7), kh8)
;     ...
;             } }
;         }
;         __syncthreads(); }
;         if (u + u_step < u_hi) SCANA_LOAD(u + u_step);
	v_cndmask_b32_e64 v20, v25, v20, s[38:39]
	v_cndmask_b32_e64 v25, v20, v75, s[38:39]
	v_cndmask_b32_e64 v20, v79, v20, s[38:39]
	v_cvt_pk_bf16_f32 v20, v25, v20
	v_add_u32_e32 v25, 0xb400, v191
	ds_write2_b32 v25, v21, v20 offset1:36
	v_mov_b32_dpp v20, v68 row_ror:8 row_mask:0xf bank_mask:0xf bound_ctrl:1
	v_mov_b32_dpp v21, v58 row_ror:8 row_mask:0xf bank_mask:0xf bound_ctrl:1
	v_cndmask_b32_e64 v20, v21, v20, s[38:39]
	v_cndmask_b32_e64 v21, v20, v68, s[38:39]
	v_cndmask_b32_e64 v20, v58, v20, s[38:39]
	v_cvt_pk_bf16_f32 v20, v21, v20
	v_add_u32_e32 v21, 0xd800, v191
	ds_write2_b32 v21, v22, v20 offset1:36
	v_mov_b32_dpp v20, v24 row_ror:8 row_mask:0xf bank_mask:0xf bound_ctrl:1
	v_mov_b32_dpp v22, v40 row_ror:8 row_mask:0xf bank_mask:0xf bound_ctrl:1
	v_cndmask_b32_e64 v20, v22, v20, s[38:39]
	v_cndmask_b32_e64 v22, v20, v24, s[38:39]
	v_cndmask_b32_e64 v20, v40, v20, s[38:39]
	v_cvt_pk_bf16_f32 v20, v22, v20
	v_add_u32_e32 v22, 0xfc00, v191
	ds_write2_b32 v22, v23, v20 offset1:36
	v_mov_b32_dpp v20, v29 row_ror:8 row_mask:0xf bank_mask:0xf bound_ctrl:1
	v_mov_b32_dpp v23, v45 row_ror:8 row_mask:0xf bank_mask:0xf bound_ctrl:1
	v_cndmask_b32_e64 v20, v23, v20, s[38:39]
	v_lshlrev_b32_e32 v76, 16, v17
	v_lshlrev_b32_e32 v80, 16, v19
	v_cndmask_b32_e64 v23, v20, v29, s[38:39]
	v_cndmask_b32_e64 v20, v45, v20, s[38:39]
	v_cvt_pk_bf16_f32 v20, v23, v20
	v_mov_b32_dpp v23, v76 row_ror:8 row_mask:0xf bank_mask:0xf bound_ctrl:1
	v_mov_b32_dpp v24, v80 row_ror:8 row_mask:0xf bank_mask:0xf bound_ctrl:1
	v_cndmask_b32_e64 v23, v24, v23, s[38:39]
	v_cndmask_b32_e64 v24, v23, v76, s[38:39]
	v_cndmask_b32_e64 v23, v80, v23, s[38:39]
	v_cvt_pk_bf16_f32 v23, v24, v23
	v_mov_b32_dpp v24, v66 row_ror:8 row_mask:0xf bank_mask:0xf bound_ctrl:1
	v_mov_b32_dpp v27, v56 row_ror:8 row_mask:0xf bank_mask:0xf bound_ctrl:1
	v_cndmask_b32_e64 v24, v27, v24, s[38:39]
	v_cndmask_b32_e64 v27, v24, v66, s[38:39]
	v_cndmask_b32_e64 v24, v56, v24, s[38:39]
	v_cvt_pk_bf16_f32 v24, v27, v24
	v_mov_b32_dpp v27, v28 row_ror:8 row_mask:0xf bank_mask:0xf bound_ctrl:1
	v_mov_b32_dpp v29, v44 row_ror:8 row_mask:0xf bank_mask:0xf bound_ctrl:1
	v_cndmask_b32_e64 v27, v29, v27, s[38:39]
	v_cndmask_b32_e64 v28, v27, v28, s[38:39]
	v_cndmask_b32_e64 v27, v44, v27, s[38:39]
	v_cvt_pk_bf16_f32 v27, v28, v27
	v_mov_b32_dpp v28, v33 row_ror:8 row_mask:0xf bank_mask:0xf bound_ctrl:1
	v_mov_b32_dpp v29, v49 row_ror:8 row_mask:0xf bank_mask:0xf bound_ctrl:1
	v_cndmask_b32_e64 v28, v29, v28, s[38:39]
	v_cndmask_b32_e64 v29, v28, v33, s[38:39]
	v_cndmask_b32_e64 v28, v49, v28, s[38:39]
	v_and_b32_e32 v77, 0xffff0000, v17
	v_and_b32_e32 v81, 0xffff0000, v19
	v_cvt_pk_bf16_f32 v28, v29, v28
	ds_write2_b32 v26, v20, v28 offset0:72 offset1:108
	v_mov_b32_dpp v20, v77 row_ror:8 row_mask:0xf bank_mask:0xf bound_ctrl:1
	v_mov_b32_dpp v26, v81 row_ror:8 row_mask:0xf bank_mask:0xf bound_ctrl:1
	v_cndmask_b32_e64 v20, v26, v20, s[38:39]
	v_cndmask_b32_e64 v26, v20, v77, s[38:39]
	v_cndmask_b32_e64 v20, v81, v20, s[38:39]
	v_cvt_pk_bf16_f32 v20, v26, v20
	ds_write2_b32 v25, v23, v20 offset0:72 offset1:108
	v_mov_b32_dpp v23, v54 row_ror:8 row_mask:0xf bank_mask:0xf bound_ctrl:1
	v_mov_b32_dpp v20, v62 row_ror:8 row_mask:0xf bank_mask:0xf bound_ctrl:1
	v_cndmask_b32_e64 v20, v23, v20, s[38:39]
	v_cndmask_b32_e64 v23, v20, v62, s[38:39]
	v_cndmask_b32_e64 v20, v54, v20, s[38:39]
	v_cvt_pk_bf16_f32 v20, v23, v20
	ds_write2_b32 v21, v24, v20 offset0:72 offset1:108
	v_mov_b32_dpp v21, v48 row_ror:8 row_mask:0xf bank_mask:0xf bound_ctrl:1
	v_mov_b32_dpp v20, v32 row_ror:8 row_mask:0xf bank_mask:0xf bound_ctrl:1
	v_readlane_b32 s40, v254, 23
	v_cndmask_b32_e64 v20, v21, v20, s[38:39]
	s_cmp_ge_i32 s62, s40
	v_cndmask_b32_e64 v21, v20, v32, s[38:39]
	v_cndmask_b32_e64 v20, v48, v20, s[38:39]
	s_cselect_b64 s[54:55], -1, 0
	v_cvt_pk_bf16_f32 v20, v21, v20
	s_and_b64 vcc, exec, s[54:55]
	ds_write2_b32 v22, v27, v20 offset0:72 offset1:108
	s_waitcnt lgkmcnt(0)
	s_barrier
	s_cbranch_vccnz .LBB0_1064
	v_mov_b32_e32 v1, v123
	s_and_b32 s43, s67, 0xffffffc0
	v_ashrrev_i32_e32 v0, 3, v1
	v_and_b32_e32 v3, 63, v1
	v_and_b32_e32 v2, -8, v0
	s_and_b32 s57, s63, 0x1c0
	s_and_b32 s42, s68, 0x6000
	s_ashr_i32 s56, s43, 31
	s_lshl_b32 s40, s57, 1
	v_lshlrev_b32_e32 v64, 1, v3
	v_ashrrev_i32_e32 v3, 31, v2
	s_add_u32 s40, s46, s40
	v_lshlrev_b64 v[6:7], 10, v[2:3]
	v_or_b32_e32 v8, 1, v2
	v_or_b32_e32 v10, 2, v2
	v_or_b32_e32 v12, 3, v2
	v_or_b32_e32 v14, 4, v2
	v_or_b32_e32 v16, 5, v2
	v_or_b32_e32 v2, 6, v2
	v_or_b32_e32 v18, 7, v0
	s_addc_u32 s41, s47, 0
	v_ashrrev_i32_e32 v9, 31, v8
	v_ashrrev_i32_e32 v11, 31, v10
	v_ashrrev_i32_e32 v13, 31, v12
	v_ashrrev_i32_e32 v15, 31, v14
	v_ashrrev_i32_e32 v17, 31, v16
	v_ashrrev_i32_e32 v3, 31, v2
	v_ashrrev_i32_e32 v19, 31, v18
	v_lshl_add_u64 v[4:5], s[40:41], 0, v[64:65]
	v_lshlrev_b64 v[8:9], 10, v[8:9]
	v_lshlrev_b64 v[10:11], 10, v[10:11]
	v_lshlrev_b64 v[12:13], 10, v[12:13]
	v_lshlrev_b64 v[14:15], 10, v[14:15]
	v_lshlrev_b64 v[16:17], 10, v[16:17]
	v_lshlrev_b64 v[2:3], 10, v[2:3]
	v_lshlrev_b64 v[18:19], 10, v[18:19]
	v_lshl_add_u64 v[6:7], v[4:5], 0, v[6:7]
	v_lshl_add_u64 v[8:9], v[4:5], 0, v[8:9]
	v_lshl_add_u64 v[10:11], v[4:5], 0, v[10:11]
	v_lshl_add_u64 v[12:13], v[4:5], 0, v[12:13]
	v_lshl_add_u64 v[14:15], v[4:5], 0, v[14:15]
	v_lshl_add_u64 v[16:17], v[4:5], 0, v[16:17]
	v_lshl_add_u64 v[2:3], v[4:5], 0, v[2:3]
	v_lshl_add_u64 v[4:5], v[4:5], 0, v[18:19]
	s_add_u32 s40, s42, s43
	v_lshlrev_b32_e32 v1, 3, v1
	global_load_ushort v20, v[8:9], off
	global_load_ushort v21, v[10:11], off
	global_load_ushort v22, v[12:13], off
	global_load_ushort v23, v[14:15], off
	global_load_ushort v24, v[16:17], off
	global_load_ushort v25, v[2:3], off
	global_load_ushort v26, v[4:5], off
	global_load_ushort v27, v[6:7], off
	s_addc_u32 s41, 0, s56
	v_and_b32_e32 v4, 56, v1
	v_ashrrev_i32_e32 v1, 31, v0
	v_lshl_add_u64 v[2:3], s[40:41], 0, v[0:1]
	v_lshlrev_b64 v[2:3], 9, v[2:3]
	v_or3_b32 v2, v2, s57, v4
	v_readlane_b32 s40, v252, 47
	v_lshlrev_b64 v[16:17], 1, v[2:3]
	v_readlane_b32 s41, v252, 48
	v_lshlrev_b64 v[8:9], 9, v[0:1]
	v_or3_b32 v8, v8, s57, v4
	v_lshl_add_u64 v[0:1], s[40:41], 0, v[16:17]
	v_readlane_b32 s40, v252, 49
	v_readlane_b32 s41, v252, 50
	v_lshlrev_b64 v[8:9], 1, v[8:9]
	v_lshl_add_u64 v[10:11], s[48:49], 0, v[8:9]
	v_lshl_add_u64 v[4:5], s[40:41], 0, v[16:17]
	v_readlane_b32 s40, v255, 7
	v_readlane_b32 s41, v255, 8
	v_lshl_add_u64 v[12:13], s[50:51], 0, v[8:9]
	global_load_dwordx4 v[0:3], v[0:1], off
	s_nop 0
	global_load_dwordx4 v[4:7], v[4:5], off
	v_lshl_add_u64 v[16:17], s[40:41], 0, v[16:17]
	global_load_dwordx4 v[8:11], v[10:11], off
	s_nop 0
	global_load_dwordx4 v[12:15], v[12:13], off
	s_waitcnt vmcnt(11)
	v_lshlrev_b32_e32 v107, 16, v20
	global_load_dwordx4 v[16:19], v[16:17], off
	s_waitcnt vmcnt(10)
	v_lshlrev_b32_e32 v109, 16, v22
	v_lshlrev_b32_e32 v106, 16, v21
	s_waitcnt vmcnt(8)
	v_lshlrev_b32_e32 v111, 16, v24
	v_lshlrev_b32_e32 v108, 16, v23
	s_waitcnt vmcnt(6)
	v_lshlrev_b32_e32 v113, 16, v26
	s_waitcnt vmcnt(5)
	v_lshlrev_b32_e32 v64, 16, v27
	v_lshlrev_b32_e32 v110, 16, v25

; #define LAS __attribute__((address_space(3)))
; #define GAS __attribute__((address_space(1)))
;     DI unsigned char* wsp() const { return (unsigned char*)ws_g; }
;     DI const float* inp(int i) const { return (const float*)(*(const GAS float* const __attribute__((address_space(4)))*)(ka + 8 * i)); }
; DI void scanc_load(ScanCIn& o, const unsigned char* ws, GAS unsigned* flags, int item, int r16, int g, int l) {
;     ...
;     const int u = item >> 2, it = item & 3; const int bh = u & 31, c = u >> 5; const size_t ui = (size_t)(bh * 128 + c);
;     {
;       GAS unsigned* fw = flags + 64 * bh; const unsigned need = 4u * ((unsigned)(c >> 2) + 1u); unsigned spins = 0;
;       while ((unsigned)__builtin_amdgcn_readfirstlane((int)__hip_atomic_load(fw, __ATOMIC_RELAXED, __HIP_MEMORY_SCOPE_AGENT)) < need) { __builtin_amdgcn_s_sleep(24); if (++spins > (1u << 20)) break; }
; DI void phase_scan_c(Frame& F, int l, int nskip) {
;     const int lane = F.lane, r16 = lane & 15, g = lane >> 4;
;     const int first = (F.bid - nskip) * 8 + F.wave, stride = (F.G - nskip) * 8;
;     { LAS float* LN = (LAS float*)F.lds; const int c = F.lane + 64 * F.wave;
;       __syncthreads(); LN[c] = F.inp(17)[l * CW + c]; LN[512 + c] = F.inp(18)[l * CW + c]; LN[1024 + c] = F.inp(16)[l * CW + c]; __syncthreads(); }
;     if (first >= NUNIT * 4) return;
;     GAS unsigned* flags = (GAS unsigned*)(F.ws_g + WS_CTL) + CW_SFLG + 64 * (l * 32);
;     ScanCIn o0, o1;
;     scanc_load(o0, F.wsp(), flags, first, r16, g, l);
.LBB0_1223:
	s_mul_i32 s0, s50, 19
	s_add_i32 s2, s0, 4
	s_cmp_le_i32 s96, s2
	s_cselect_b64 s[0:1], -1, 0
	s_cmp_lt_i32 s2, s97
	s_cselect_b64 s[2:3], -1, 0
	s_and_b64 s[0:1], s[0:1], s[2:3]
	s_andn2_b64 vcc, exec, s[0:1]
	v_readlane_b32 s0, v252, 17
	v_readlane_b32 s1, v252, 18
	v_readlane_b32 s4, v252, 19
	v_readlane_b32 s5, v252, 20
	v_writelane_b32 v252, s0, 17
	s_nop 1
	v_writelane_b32 v252, s1, 18
	v_writelane_b32 v252, s4, 19
	s_nop 1
	v_writelane_b32 v252, s5, 20
	s_cbranch_vccnz .LBB0_1273
	s_cmp_lt_i32 s88, 32
	s_cselect_b64 s[2:3], -1, 0
	s_cmp_gt_i32 s4, 64
	s_cselect_b64 s[0:1], -1, 0
	s_and_b64 s[2:3], s[2:3], s[0:1]
	s_add_u32 s20, s94, 0xc000
	s_addc_u32 s21, s95, 0
	s_lshl_b32 s4, s50, 11
	s_add_u32 s22, s94, 0x12200000
	s_addc_u32 s23, s95, 0
	v_mov_b32_e32 v196, v230
	s_andn2_b64 vcc, exec, s[2:3]
	s_mov_b64 s[2:3], -1
	s_cbranch_vccz .LBB0_1248
	s_andn2_b64 vcc, exec, s[0:1]
	s_cbranch_vccnz .LBB0_1247
	s_waitcnt vmcnt(0)
	v_lshl_add_u32 v4, s68, 6, v196
	s_waitcnt vmcnt(0) lgkmcnt(0)
	s_barrier
	s_load_dwordx4 s[0:3], s[90:91], 0x80
	s_load_dwordx2 s[6:7], s[90:91], 0x90
	v_lshl_add_u32 v0, s50, 9, v4
	v_ashrrev_i32_e32 v1, 31, v0
	v_lshlrev_b64 v[0:1], 2, v[0:1]
	s_waitcnt lgkmcnt(0)
	v_lshl_add_u64 v[2:3], s[2:3], 0, v[0:1]
	global_load_dword v5, v[2:3], off
	v_lshl_add_u64 v[2:3], s[6:7], 0, v[0:1]
	global_load_dword v2, v[2:3], off
	v_lshl_add_u64 v[0:1], s[0:1], 0, v[0:1]
	global_load_dword v0, v[0:1], off
	s_lshl_b32 s0, s88, 3
	s_add_i32 s0, s0, s68
	s_add_i32 s25, s0, 0xffffff00
	v_lshl_add_u32 v1, v4, 2, s83
	s_cmpk_gt_i32 s25, 0x3fff
	s_waitcnt vmcnt(1)
	ds_write2st64_b32 v1, v5, v2 offset1:8
	s_waitcnt vmcnt(0)
	ds_write_b32 v1, v0 offset:4096
	s_waitcnt lgkmcnt(0)
	s_barrier
	s_cbranch_scc1 .LBB0_1247
	s_mov_b32 s5, s45
	s_lshl_b64 s[0:1], s[4:5], 2
	s_add_u32 s5, s20, s0
	s_mov_b32 s14, s25
	s_addc_u32 s18, s21, s1
	s_bfe_u32 s12, s14, 0x50002
	s_lshr_b32 s15, s14, 2
	s_ashr_i32 s13, s14, 7
	s_lshl_b32 s0, s12, 8
	s_add_u32 s0, s5, s0
	s_addc_u32 s1, s18, 0
	s_and_b32 s6, s13, -4
	s_add_i32 s6, s6, 4
	s_mov_b32 s7, 0x100001
	s_mov_b32 s98, 0
	s_mov_b32 s99, -1
	s_branch .LBB0_1229

; #define GAS __attribute__((address_space(1)))
; DI void scanc_load(ScanCIn& o, const unsigned char* ws, GAS unsigned* flags, int item, int r16, int g, int l) {
;     ...
;       GAS unsigned* fw = flags + 64 * bh; const unsigned need = 4u * ((unsigned)(c >> 2) + 1u); unsigned spins = 0;
;       while ((unsigned)__builtin_amdgcn_readfirstlane((int)__hip_atomic_load(fw, __ATOMIC_RELAXED, __HIP_MEMORY_SCOPE_AGENT)) < need) { __builtin_amdgcn_s_sleep(24); if (++spins > (1u << 20)) break; }
;       asm volatile("" ::: "memory"); }
.LBB0_1229:
	s_cmp_lg_u32 s99, s12
	s_cselect_b32 s98, 0, s98
	s_mov_b32 s99, s12
	s_cmp_ge_u32 s98, s6
	s_mov_b64 s[2:3], -1
	s_cbranch_scc1 .LBB0_1228
	global_load_dword v0, v65, s[0:1] sc1
	s_waitcnt vmcnt(0)
	v_readfirstlane_b32 s2, v0
	s_mov_b32 s98, s2
	s_cmp_ge_u32 s2, s6
	s_mov_b64 s[2:3], -1
	s_cbranch_scc1 .LBB0_1228
	s_add_i32 s7, s7, -1
	s_cmp_eq_u32 s7, 0
	s_cselect_b64 s[2:3], -1, 0
	s_sleep 24
	s_branch .LBB0_1228

; #define GAS __attribute__((address_space(1)))
; DI void scanc_load(ScanCIn& o, const unsigned char* ws, GAS unsigned* flags, int item, int r16, int g, int l) {
;     ...
;       GAS unsigned* fw = flags + 64 * bh; const unsigned need = 4u * ((unsigned)(c >> 2) + 1u); unsigned spins = 0;
;       while ((unsigned)__builtin_amdgcn_readfirstlane((int)__hip_atomic_load(fw, __ATOMIC_RELAXED, __HIP_MEMORY_SCOPE_AGENT)) < need) { __builtin_amdgcn_s_sleep(24); if (++spins > (1u << 20)) break; }
;       asm volatile("" ::: "memory"); }
.LBB0_1238:
	s_cmp_lg_u32 s99, s28
	s_cselect_b32 s98, 0, s98
	s_mov_b32 s99, s28
	s_cmp_ge_u32 s98, s30
	s_mov_b64 s[16:17], -1
	s_cbranch_scc1 .LBB0_1237
	global_load_dword v16, v65, s[14:15] sc1
	s_waitcnt vmcnt(0)
	v_readfirstlane_b32 s16, v16
	s_mov_b32 s98, s16
	s_cmp_ge_u32 s16, s30
	s_mov_b64 s[16:17], -1
	s_cbranch_scc1 .LBB0_1237
	s_add_i32 s31, s31, -1
	s_cmp_eq_u32 s31, 0
	s_cselect_b64 s[16:17], -1, 0
	s_sleep 24
	s_branch .LBB0_1237

; #define GAS __attribute__((address_space(1)))
; DI void scanc_load(ScanCIn& o, const unsigned char* ws, GAS unsigned* flags, int item, int r16, int g, int l) {
;     ...
;       GAS unsigned* fw = flags + 64 * bh; const unsigned need = 4u * ((unsigned)(c >> 2) + 1u); unsigned spins = 0;
;       while ((unsigned)__builtin_amdgcn_readfirstlane((int)__hip_atomic_load(fw, __ATOMIC_RELAXED, __HIP_MEMORY_SCOPE_AGENT)) < need) { __builtin_amdgcn_s_sleep(24); if (++spins > (1u << 20)) break; }
;       asm volatile("" ::: "memory"); }
.LBB0_1245:
	s_cmp_lg_u32 s99, s26
	s_cselect_b32 s98, 0, s98
	s_mov_b32 s99, s26
	s_cmp_ge_u32 s98, s28
	s_mov_b64 s[14:15], -1
	s_cbranch_scc1 .LBB0_1244
	global_load_dword v0, v65, s[12:13] sc1
	s_waitcnt vmcnt(0)
	v_readfirstlane_b32 s14, v0
	s_mov_b32 s98, s14
	s_cmp_ge_u32 s14, s28
	s_mov_b64 s[14:15], -1
	s_cbranch_scc1 .LBB0_1244
	s_add_i32 s29, s29, -1
	s_cmp_eq_u32 s29, 0
	s_cselect_b64 s[14:15], -1, 0
	s_sleep 24
	s_branch .LBB0_1244
